# agg gather: removed the now-dead per-edge relation-count SALU (5 scalar ops per edge)
# speedup vs baseline: 1.0132x; 1.0018x over previous
.Lagg_ld7:
	s_add_u32 s17, s15, 7
	v_readlane_b32 s28, v6, s17
	s_mul_i32 s29, s28, 0x220
	s_add_u32 s54, s26, s29
	s_addc_u32 s55, s27, 0
	global_load_dwordx2 v[54:55], v8, s[54:55]
	global_load_dword v39, v20, s[54:55] offset:512
.Lagg_ld6:
	s_add_u32 s17, s15, 6
	v_readlane_b32 s28, v6, s17
	s_mul_i32 s29, s28, 0x220
	s_add_u32 s52, s26, s29
	s_addc_u32 s53, s27, 0
	global_load_dwordx2 v[52:53], v8, s[52:53]
	global_load_dword v38, v20, s[52:53] offset:512
.Lagg_ld5:
	s_add_u32 s17, s15, 5
	v_readlane_b32 s28, v6, s17
	s_mul_i32 s29, s28, 0x220
	s_add_u32 s50, s26, s29
	s_addc_u32 s51, s27, 0
	global_load_dwordx2 v[50:51], v8, s[50:51]
	global_load_dword v37, v20, s[50:51] offset:512
.Lagg_ld4:
	s_add_u32 s17, s15, 4
	v_readlane_b32 s28, v6, s17
	s_mul_i32 s29, s28, 0x220
	s_add_u32 s48, s26, s29
	s_addc_u32 s49, s27, 0
	global_load_dwordx2 v[48:49], v8, s[48:49]
	global_load_dword v36, v20, s[48:49] offset:512
.Lagg_ld3:
	s_add_u32 s17, s15, 3
	v_readlane_b32 s28, v6, s17
	s_mul_i32 s29, s28, 0x220
	s_add_u32 s46, s26, s29
	s_addc_u32 s47, s27, 0
	global_load_dwordx2 v[46:47], v8, s[46:47]
	global_load_dword v35, v20, s[46:47] offset:512
.Lagg_ld2:
	s_add_u32 s17, s15, 2
	v_readlane_b32 s28, v6, s17
	s_mul_i32 s29, s28, 0x220
	s_add_u32 s44, s26, s29
	s_addc_u32 s45, s27, 0
	global_load_dwordx2 v[44:45], v8, s[44:45]
	global_load_dword v34, v20, s[44:45] offset:512
.Lagg_ld1:
	s_add_u32 s17, s15, 1
	v_readlane_b32 s28, v6, s17
	s_mul_i32 s29, s28, 0x220
	s_add_u32 s42, s26, s29
	s_addc_u32 s43, s27, 0
	global_load_dwordx2 v[42:43], v8, s[42:43]
	global_load_dword v33, v20, s[42:43] offset:512
.Lagg_ld0:
	s_add_u32 s17, s15, 0
	v_readlane_b32 s28, v6, s17
	s_mul_i32 s29, s28, 0x220
	s_add_u32 s40, s26, s29
	s_addc_u32 s41, s27, 0
	global_load_dwordx2 v[40:41], v8, s[40:41]
	global_load_dword v32, v20, s[40:41] offset:512
	s_cmp_ge_u32 s16, 8
	s_cbranch_scc1 .Lagg_ac7
	s_cmp_ge_u32 s16, 7
	s_cbranch_scc1 .Lagg_ac6
	s_cmp_ge_u32 s16, 6
	s_cbranch_scc1 .Lagg_ac5
	s_cmp_ge_u32 s16, 5
	s_cbranch_scc1 .Lagg_ac4
	s_cmp_ge_u32 s16, 4
	s_cbranch_scc1 .Lagg_ac3
	s_cmp_ge_u32 s16, 3
	s_cbranch_scc1 .Lagg_ac2
	s_cmp_ge_u32 s16, 2
	s_cbranch_scc1 .Lagg_ac1
	s_branch .Lagg_ac0
